# v13: hand-written router row body (params in registers per block, single pass) + 128 router / 128 sweeper workgroups in P13
# baseline (speedup 1.0000x reference)
; __device__ __forceinline__ void phase_router(const Ctx& P, LAS unsigned char* lds, int vcu, int G) {
;     ...
;     for (int blk = vcu; blk < ML / 32; blk += G) {
;         if (tid < 8) lcnt[tid] = 0;
;         for (int q = 0; q < 4; ++q) {
; __global__ void __launch_bounds__(512, 2) fwd_kernel(Params KP) {
;     ...
;         if (vcu & 1) { phase_router(P, lds, vcu, G); __syncthreads(); tr_slack(P, lds, (unsigned*)(ws + WS_CTL) + CW_TILE, nullptr, 0u); }
.LBB0_2342:
	s_or_b64 exec, exec, s[2:3]
	v_and_b32_e32 v1, 63, v0
	v_readfirstlane_b32 s12, v0
	s_cmpk_gt_i32 s33, 0x1ff
	v_lshlrev_b32_e32 v74, 2, v1
	s_waitcnt lgkmcnt(0)
	s_barrier
	s_cbranch_scc1 .LBB0_2377
	v_mov_b64_e32 v[2:3], s[28:29]
	flat_load_dwordx2 v[2:3], v[2:3] offset:56
	s_add_u32 s9, s36, 0x13c000
	v_mov_b32_e32 v11, 0
	v_mbcnt_lo_u32_b32 v7, -1, 0
	v_lshlrev_b32_e32 v10, 8, v0
	s_addc_u32 s38, s37, 0
	s_mov_b64 s[14:15], 0x4000
	v_mbcnt_hi_u32_b32 v7, -1, v7
	v_lshl_add_u64 v[12:13], s[36:37], 0, v[10:11]
	s_add_u32 s30, s36, 0x200000
	v_and_b32_e32 v9, 64, v7
	v_lshl_add_u64 v[12:13], v[12:13], 0, s[14:15]
	s_addc_u32 s31, s37, 0
	s_lshr_b32 s14, s12, 4
	v_xor_b32_e32 v14, 1, v7
	s_add_i32 s13, 0, 0x20700
	v_add_u32_e32 v9, 64, v9
	s_and_b32 s46, s14, 0xffffffc
	v_lshlrev_b32_e32 v5, 2, v0
	v_xor_b32_e32 v15, 2, v7
	v_cmp_lt_i32_e32 vcc, v14, v9
	s_add_u32 s47, s36, 0x1c2c0000
	v_add_u32_e32 v62, s13, v5
	v_cndmask_b32_e32 v14, v7, v14, vcc
	v_cmp_lt_i32_e32 vcc, v15, v9
	s_addc_u32 s48, s37, 0
	s_add_i32 s72, 0, 0x20600
	s_add_i32 s71, 0, 0x20400
	s_add_i32 s13, 0, 0x20740
	s_add_i32 s15, 0, 0x20500
	s_mov_b64 s[10:11], 0x2000
	v_cndmask_b32_e32 v15, v7, v15, vcc
	s_add_u32 s34, s36, 0x5cf30000
	v_lshlrev_b32_e32 v63, 2, v14
	v_lshlrev_b32_e32 v64, 2, v15
	s_addc_u32 s35, s37, 0
	s_add_i32 s76, 0, 0x10000
	s_add_i32 s68, 0, 0x20760
	v_xor_b32_e32 v16, 4, v7
	v_lshlrev_b32_e32 v10, 4, v1
	v_xor_b32_e32 v17, 8, v7
	v_cmp_lt_i32_e32 vcc, v16, v9
	v_add_u32_e32 v69, s72, v5
	v_add_u32_e32 v70, s71, v5
	v_xor_b32_e32 v25, 16, v7
	v_cndmask_b32_e32 v16, v7, v16, vcc
	v_cmp_lt_i32_e32 vcc, v17, v9
	v_lshl_add_u64 v[32:33], s[36:37], 0, v[10:11]
	v_xor_b32_e32 v26, 32, v7
	v_cndmask_b32_e32 v17, v7, v17, vcc
	v_cmp_lt_i32_e32 vcc, v25, v9
	v_or_b32_e32 v4, 0x100, v74
	v_or_b32_e32 v6, 0x200, v74
	v_or_b32_e32 v8, 0x300, v74
	v_or_b32_e32 v34, 0x400, v74
	v_cndmask_b32_e32 v25, v7, v25, vcc
	v_cmp_lt_i32_e32 vcc, v26, v9
	v_or_b32_e32 v36, 0x600, v74
	v_or_b32_e32 v38, 0x700, v74
	v_and_b32_e32 v58, 1, v0
	v_lshlrev_b32_e32 v18, 2, v4
	v_mov_b32_e32 v19, v11
	v_lshlrev_b32_e32 v20, 2, v6
	v_mov_b32_e32 v21, v11
	v_lshlrev_b32_e32 v22, 2, v8
	v_mov_b32_e32 v23, v11
	v_lshlrev_b32_e32 v24, 2, v34
	v_cndmask_b32_e32 v7, v7, v26, vcc
	v_lshlrev_b32_e32 v67, 2, v25
	v_mov_b32_e32 v25, v11
	v_mov_b32_e32 v27, v11
	v_lshlrev_b32_e32 v28, 2, v36
	v_mov_b32_e32 v29, v11
	v_lshlrev_b32_e32 v30, 2, v38
	v_mov_b32_e32 v31, v11
	v_cmp_gt_u32_e64 s[2:3], 8, v0
	v_cmp_eq_u32_e64 s[4:5], 0, v1
	v_cmp_gt_u32_e64 s[6:7], 64, v0
	v_and_b32_e32 v59, 0xf8, v5
	v_lshlrev_b32_e32 v60, 1, v58
	s_waitcnt vmcnt(0) lgkmcnt(0)
	v_lshl_add_u64 v[14:15], v[2:3], 0, s[10:11]
	s_lshl_b32 s10, s46, 11
	s_add_i32 s49, s76, s10
	s_lshl_b32 s10, s46, 2
	s_add_i32 s50, s68, s10
	s_lshl_b32 s10, s46, 3
	s_add_i32 s51, s71, s10
	s_add_i32 s52, s72, s10
	s_or_b32 s10, s10, 4
	s_add_i32 s53, s71, s10
	s_add_i32 s54, s72, s10
	s_or_b32 s10, s46, 1
	s_lshl_b32 s11, s10, 11
	s_add_i32 s55, s76, s11
	s_lshl_b32 s11, s10, 2
	s_lshl_b32 s10, s10, 3
	s_add_i32 s57, s71, s10
	s_add_i32 s58, s72, s10
	s_or_b32 s10, s10, 4
	s_add_i32 s59, s71, s10
	s_add_i32 s60, s72, s10
	s_or_b32 s10, s46, 2
	s_add_i32 s56, s68, s11
	s_lshl_b32 s11, s10, 11
	s_add_i32 s61, s76, s11
	s_lshl_b32 s11, s10, 2
	s_lshl_b32 s10, s10, 3
	s_add_i32 s63, s71, s10
	s_add_i32 s64, s72, s10
	s_or_b32 s10, s10, 4
	s_add_i32 s65, s71, s10
	s_add_i32 s66, s72, s10
	s_or_b32 s10, s14, 3
	s_add_i32 s62, s68, s11
	s_lshl_b32 s11, s10, 11
	s_add_i32 s67, s76, s11
	s_lshl_b32 s11, s10, 2
	s_lshl_b32 s10, s10, 3
	s_add_i32 s69, s71, s10
	s_add_i32 s70, s72, s10
	s_or_b32 s10, s10, 4
	s_add_i32 s68, s68, s11
	s_add_i32 s71, s71, s10
	s_add_i32 s72, s72, s10
	s_mov_b64 s[10:11], 0x4aec0000
	s_add_u32 s73, s36, 0x1c2c0200
	v_lshl_add_u64 v[32:33], v[32:33], 0, s[10:11]
	s_addc_u32 s74, s37, 0
	s_lshl_b32 s10, s33, 4
	s_andn2_b32 s10, s10, 16
	v_or_b32_e32 v2, 0x500, v74
	s_add_i32 s40, s10, s46
	s_lshl_b32 s10, s12, 7
	v_lshlrev_b32_e32 v26, 2, v2
	s_and_b32 s10, s10, 0xffffe000
	v_add_u32_e32 v61, 0, v10
	v_lshlrev_b32_e32 v65, 2, v16
	v_lshlrev_b32_e32 v66, 2, v17
	v_lshlrev_b32_e32 v68, 2, v7
	v_add_u32_e32 v71, s13, v5
	v_add_u32_e32 v72, s15, v5
	v_lshl_add_u64 v[16:17], v[14:15], 0, v[10:11]
	v_lshl_add_u64 v[18:19], v[14:15], 0, v[18:19]
	v_lshl_add_u64 v[20:21], v[14:15], 0, v[20:21]
	v_lshl_add_u64 v[22:23], v[14:15], 0, v[22:23]
	v_lshl_add_u64 v[24:25], v[14:15], 0, v[24:25]
	v_lshl_add_u64 v[26:27], v[14:15], 0, v[26:27]
	v_lshl_add_u64 v[28:29], v[14:15], 0, v[28:29]
	v_lshl_add_u64 v[30:31], v[14:15], 0, v[30:31]
	s_lshr_b32 s98, s39, 1
	s_lshl_b32 s75, s98, 5
	s_add_i32 s76, s76, s10
	v_mov_b32_e32 v73, 0x358637bd
	v_lshlrev_b32_e32 v75, 2, v4
	v_lshlrev_b32_e32 v76, 2, v6
	v_lshlrev_b32_e32 v77, 2, v8
	v_lshlrev_b32_e32 v78, 2, v34
	v_lshlrev_b32_e32 v79, 2, v2
	v_lshlrev_b32_e32 v80, 2, v36
	v_lshlrev_b32_e32 v81, 2, v38
	s_mov_b32 s77, 0xda24260
	s_mov_b32 s78, 0x42fe0000
	s_mov_b32 s79, 0x4b3fff81
	s_mov_b32 s80, 0xc0c0400
	s_mov_b32 s81, 0x5040100
	s_mov_b32 s82, 0xff61b1e6
	v_mov_b32_e32 v82, 1
	v_mov_b32_e32 v83, 0x4b40007f
	v_mov_b32_e32 v84, 0xff61b1e6
	s_lshr_b32 s83, s33, 1
	s_branch .LBB0_2345
